# P4 cross-attention tile loop: K and V LDS fragments read ahead of their MFMAs into unused registers with counted lgkmcnt waits
# speedup vs baseline: 1.0013x; 1.0013x over previous
; #define LAS __attribute__((address_space(3)))
; __device__ __forceinline__ unsigned cvtpk(float lo, float hi) { typedef __bf16 bf16x2_t __attribute__((ext_vector_type(2))); f32x2 v = {lo, hi}; bf16x2_t b = __builtin_convertvector(v, bf16x2_t); return __builtin_bit_cast(unsigned, b); }
; __device__ __forceinline__ s16x4 vtr(const LAS unsigned char* p) { return __builtin_bit_cast(s16x4, __builtin_amdgcn_ds_read_tr16_b64_v4i16((LAS v4i16_t*)p)); }
; template <int D, bool MASK, bool BIAS, bool SINK, bool REV, bool O8, class BG>
; __device__ __forceinline__ void attn_unit(const Prm& P, LAS unsigned char* lds, BG& bg) {
;     ...
;             float sacc = 0.f;
; #pragma unroll
;             for (int r = 0; r < 16; ++r) { p0[r] = __builtin_amdgcn_exp2f(p0[r]); p1[r] = __builtin_amdgcn_exp2f(p1[r]); sacc += p0[r] + p1[r]; }
;             l_reg += sacc;
;             u32x4 pw[4];
; #pragma unroll
;             for (int q = 0; q < 4; ++q) { pw[0][q] = cvtpk(p0[2 * q], p0[2 * q + 1]); pw[1][q] = cvtpk(p0[8 + 2 * q], p0[9 + 2 * q]); pw[2][q] = cvtpk(p1[2 * q], p1[2 * q + 1]); pw[3][q] = cvtpk(p1[8 + 2 * q], p1[9 + 2 * q]); }
;             const LAS unsigned char* vs = lds + VOFF + s * KSLOT + ((lane >> 4) & 1) * 32 + (lane & 3) * 8 + (4 * hi + ((lane & 15) >> 2)) * 64;
; #pragma unroll
;             for (int d = 0; d < NDB; ++d)
; #pragma unroll
;                 for (int k4 = 0; k4 < 4; ++k4) {
;                     const s16x4 vlo = vtr(vs + d * 4096 + k4 * 1024), vhi = vtr(vs + d * 4096 + k4 * 1024 + 512);
;                     const bf16x8 vf = (bf16x8){vlo[0], vlo[1], vlo[2], vlo[3], vhi[0], vhi[1], vhi[2], vhi[3]};
;                     o[d] = __builtin_amdgcn_mfma_f32_32x32x16_bf16(__builtin_bit_cast(bf16x8, pw[k4]), vf, o[d], 0, 0, 0);
;                 }
.LBB0_940:
	v_exp_f32_e32 v2, v84
	v_exp_f32_e32 v135, v68
	v_exp_f32_e32 v151, v85
	v_exp_f32_e32 v156, v69
	v_exp_f32_e32 v86, v86
	v_exp_f32_e32 v157, v70
	v_exp_f32_e32 v87, v87
	v_exp_f32_e32 v158, v71
	v_add_f32_e32 v68, v135, v2
	v_exp_f32_e32 v159, v88
	v_exp_f32_e32 v160, v72
	v_add_f32_e32 v68, 0, v68
	v_add_f32_e32 v69, v156, v151
	v_exp_f32_e32 v70, v89
	v_exp_f32_e32 v88, v73
	v_add_f32_e32 v68, v69, v68
	v_add_f32_e32 v69, v157, v86
	v_add_f32_e32 v68, v69, v68
	v_add_f32_e32 v69, v158, v87
	v_add_f32_e32 v71, v69, v68
	v_add_f32_e32 v89, v160, v159
	v_pk_add_f32 v[68:69], v[88:89], v[70:71]
	v_exp_f32_e32 v71, v90
	v_pk_add_f32 v[72:73], v[68:69], v[68:69] op_sel_hi:[0,1]
	v_exp_f32_e32 v89, v74
	v_exp_f32_e32 v72, v91
	v_exp_f32_e32 v90, v75
	v_exp_f32_e32 v161, v76
	v_add_f32_e32 v91, v89, v71
	v_cvt_pk_bf16_f32 v70, v159, v70
	v_pk_add_f32 v[68:69], v[90:91], v[72:73]
	v_exp_f32_e32 v91, v92
	v_pk_add_f32 v[84:85], v[68:69], v[68:69] op_sel_hi:[0,1]
	v_exp_f32_e32 v84, v93
	v_exp_f32_e32 v92, v77
	v_add_f32_e32 v93, v161, v91
	v_exp_f32_e32 v77, v94
	v_exp_f32_e32 v94, v79
	v_pk_add_f32 v[68:69], v[92:93], v[84:85]
	v_exp_f32_e32 v93, v78
	v_pk_add_f32 v[152:153], v[68:69], v[68:69] op_sel_hi:[0,1]
	v_exp_f32_e32 v152, v95
	v_cvt_pk_bf16_f32 v71, v71, v72
	v_add_f32_e32 v95, v93, v77
	v_cvt_pk_bf16_f32 v76, v91, v84
	v_pk_add_f32 v[68:69], v[94:95], v[152:153]
	v_exp_f32_e32 v95, v96
	v_pk_add_f32 v[78:79], v[68:69], v[68:69] op_sel_hi:[0,1]
	v_exp_f32_e32 v153, v80
	v_exp_f32_e32 v78, v97
	v_exp_f32_e32 v96, v81
	v_cvt_pk_bf16_f32 v77, v77, v152
	v_add_f32_e32 v97, v153, v95
	v_cvt_pk_bf16_f32 v80, v161, v92
	v_pk_add_f32 v[68:69], v[96:97], v[78:79]
	v_exp_f32_e32 v97, v98
	v_pk_add_f32 v[154:155], v[68:69], v[68:69] op_sel_hi:[0,1]
	v_cvt_pk_bf16_f32 v68, v2, v151
	v_add_u32_e32 v2, s74, v1
	v_cvt_pk_bf16_f32 v69, v86, v87
	s_nop 0
	ds_read_b64_tr_b16 v[72:73], v2 offset:32768
	ds_read_b64_tr_b16 v[74:75], v2 offset:33280
	v_exp_f32_e32 v154, v99
	s_waitcnt lgkmcnt(0)
	v_mfma_f32_32x32x16_bf16 v[52:67], v[68:71], v[72:75], v[52:67]
	ds_read_b64_tr_b16 v[84:85], v2 offset:33792
	ds_read_b64_tr_b16 v[86:87], v2 offset:34304
	v_cvt_pk_bf16_f32 v78, v95, v78
	v_cvt_pk_bf16_f32 v79, v97, v154
	v_cvt_pk_bf16_f32 v72, v135, v156
	v_cvt_pk_bf16_f32 v73, v157, v158
	v_cvt_pk_bf16_f32 v74, v160, v88
	v_cvt_pk_bf16_f32 v75, v89, v90
	s_waitcnt lgkmcnt(0)
	v_mfma_f32_32x32x16_bf16 v[52:67], v[76:79], v[84:87], v[52:67]
	ds_read_b64_tr_b16 v[84:85], v2 offset:34816
	ds_read_b64_tr_b16 v[86:87], v2 offset:35328
	v_exp_f32_e32 v95, v82
	v_exp_f32_e32 v98, v83
	ds_read_b64_tr_b16 v[88:89], v2 offset:35840
	ds_read_b64_tr_b16 v[90:91], v2 offset:36352
	v_cvt_pk_bf16_f32 v81, v93, v94
	v_cvt_pk_bf16_f32 v82, v153, v96
	v_cvt_pk_bf16_f32 v83, v95, v98
	s_waitcnt lgkmcnt(2)
	v_mfma_f32_32x32x16_bf16 v[52:67], v[72:75], v[84:87], v[52:67]
	v_add_f32_e32 v99, v95, v97
	s_add_i32 s73, s73, 1
	v_add_u32_e32 v147, 64, v147
	v_add_u32_e32 v150, 64, v150
	s_cmp_eq_u32 s73, 4
	s_mov_b64 s[44:45], 0
	s_waitcnt lgkmcnt(0)
	v_mfma_f32_32x32x16_bf16 v[52:67], v[80:83], v[88:91], v[52:67]
	ds_read_b64_tr_b16 v[192:193], v2 offset:36864
	ds_read_b64_tr_b16 v[194:195], v2 offset:37376
	ds_read_b64_tr_b16 v[196:197], v2 offset:37888
	ds_read_b64_tr_b16 v[198:199], v2 offset:38400
	ds_read_b64_tr_b16 v[200:201], v2 offset:38912
	ds_read_b64_tr_b16 v[202:203], v2 offset:39424
	ds_read_b64_tr_b16 v[204:205], v2 offset:39936
	ds_read_b64_tr_b16 v[206:207], v2 offset:40448
	ds_read_b64_tr_b16 v[208:209], v2 offset:40960
	ds_read_b64_tr_b16 v[210:211], v2 offset:41472
	ds_read_b64_tr_b16 v[212:213], v2 offset:41984
	ds_read_b64_tr_b16 v[214:215], v2 offset:42496
	s_waitcnt lgkmcnt(8)
	v_mfma_f32_32x32x16_bf16 v[36:51], v[68:71], v[192:195], v[36:51]
	v_mfma_f32_32x32x16_bf16 v[36:51], v[76:79], v[196:199], v[36:51]
	ds_read_b64_tr_b16 v[216:217], v2 offset:43008
	ds_read_b64_tr_b16 v[218:219], v2 offset:43520
	ds_read_b64_tr_b16 v[220:221], v2 offset:44032
	ds_read_b64_tr_b16 v[222:223], v2 offset:44544
	s_waitcnt lgkmcnt(8)
	v_mfma_f32_32x32x16_bf16 v[36:51], v[72:75], v[200:203], v[36:51]
	v_mfma_f32_32x32x16_bf16 v[36:51], v[80:83], v[204:207], v[36:51]
	ds_read_b64_tr_b16 v[224:225], v2 offset:45056
	ds_read_b64_tr_b16 v[226:227], v2 offset:45568
	ds_read_b64_tr_b16 v[228:229], v2 offset:46080
	ds_read_b64_tr_b16 v[230:231], v2 offset:46592
	s_waitcnt lgkmcnt(8)
	v_mfma_f32_32x32x16_bf16 v[20:35], v[68:71], v[208:211], v[20:35]
	v_mfma_f32_32x32x16_bf16 v[20:35], v[76:79], v[212:215], v[20:35]
	ds_read_b64_tr_b16 v[232:233], v2 offset:47104
	ds_read_b64_tr_b16 v[234:235], v2 offset:47616
	ds_read_b64_tr_b16 v[236:237], v2 offset:48128
	ds_read_b64_tr_b16 v[238:239], v2 offset:48640
	s_waitcnt lgkmcnt(8)
	v_mfma_f32_32x32x16_bf16 v[20:35], v[72:75], v[216:219], v[20:35]
	v_mfma_f32_32x32x16_bf16 v[20:35], v[80:83], v[220:223], v[20:35]
	s_waitcnt lgkmcnt(4)
	v_mfma_f32_32x32x16_bf16 v[4:19], v[68:71], v[224:227], v[4:19]
	v_mfma_f32_32x32x16_bf16 v[4:19], v[76:79], v[228:231], v[4:19]
	s_waitcnt lgkmcnt(0)
	v_mfma_f32_32x32x16_bf16 v[4:19], v[72:75], v[232:235], v[4:19]
	v_add_f32_e64 v68, v98, v154
	v_add_f32_e64 v69, v99, v155
	v_add_f32_e32 v2, v68, v69
	v_add_f32_e32 v149, v149, v2
	v_mfma_f32_32x32x16_bf16 v[4:19], v[80:83], v[236:239], v[4:19]
	s_cbranch_scc1 .LBB0_951

; #define LAS __attribute__((address_space(3)))
; __device__ __forceinline__ float max3f(float a, float b, float c) { return __builtin_fmaxf(__builtin_fmaxf(a, b), c); }
; template <int D, bool MASK, bool BIAS, bool SINK, bool REV, bool O8, class BG>
; __device__ __forceinline__ void attn_unit(const Prm& P, LAS unsigned char* lds, BG& bg) {
;     ...
;         if (compute) {
;             const float cinit = cq - mhat;
;             f32x16 p0, p1;
; #pragma unroll
;             for (int r = 0; r < 16; ++r) { p0[r] = cinit; p1[r] = cinit; }
;             const LAS unsigned char* ks = lds + KOFF + s * KSLOT + hi * 1024 + r32 * 16;
; #pragma unroll
;             for (int d0 = 0; d0 < NKS; ++d0) {
;                 const bf16x8 b0 = *(const LAS bf16x8*)(ks + d0 * 2048), b1 = *(const LAS bf16x8*)(ks + d0 * 2048 + 512);
;                 p0 = __builtin_amdgcn_mfma_f32_32x32x16_bf16(b0, qr[d0], p0, 0, 0, 0);
;                 p1 = __builtin_amdgcn_mfma_f32_32x32x16_bf16(b1, qr[d0], p1, 0, 0, 0);
;             }
;     ...
;             float a = max3f(p0[0], p0[1], p1[0]), b = max3f(p0[2], p0[3], p1[1]); a = max3f(a, p1[2], p1[3]);
; #pragma unroll
;             for (int r = 4; r < 16; r += 4) { a = max3f(a, p0[r], p0[r + 1]); b = max3f(b, p0[r + 2], p0[r + 3]); a = max3f(a, p1[r], p1[r + 1]); b = max3f(b, p1[r + 2], p1[r + 3]); }
;             float rm = __builtin_fmaxf(a, b);
;             { auto rr = __builtin_amdgcn_permlane32_swap(__float_as_uint(rm), __float_as_uint(rm), false, false); rm = __builtin_fmaxf(__uint_as_float(rr[0]), __uint_as_float(rr[1])); }
;             if (first || __any(rm > THR)) {
.LBB0_945:
	v_add_u32_e32 v2, s74, v142
	ds_read_b128 v[152:155], v2
	ds_read_b128 v[156:159], v2 offset:512
	ds_read_b128 v[192:195], v2 offset:2048
	ds_read_b128 v[196:199], v2 offset:2560
	ds_read_b128 v[200:203], v2 offset:4096
	ds_read_b128 v[204:207], v2 offset:4608
	ds_read_b128 v[208:211], v2 offset:6144
	ds_read_b128 v[212:215], v2 offset:6656
	ds_read_b128 v[216:219], v2 offset:8192
	ds_read_b128 v[220:223], v2 offset:8704
	ds_read_b128 v[224:227], v2 offset:10240
	ds_read_b128 v[228:231], v2 offset:10752
	ds_read_b128 v[232:235], v2 offset:12288
	ds_read_b128 v[236:239], v2 offset:12800
	v_sub_f32_e32 v68, 0, v148
	v_mov_b32_e32 v69, v68
	v_mov_b32_e32 v70, v68
	v_mov_b32_e32 v71, v68
	v_mov_b32_e32 v72, v68
	v_mov_b32_e32 v73, v68
	v_mov_b32_e32 v74, v68
	v_mov_b32_e32 v75, v68
	v_mov_b32_e32 v76, v68
	v_mov_b32_e32 v77, v68
	v_mov_b32_e32 v78, v68
	v_mov_b32_e32 v79, v68
	v_mov_b32_e32 v80, v68
	v_mov_b32_e32 v81, v68
	v_mov_b32_e32 v82, v68
	v_mov_b32_e32 v83, v68
	s_xor_b64 s[46:47], s[44:45], -1
	s_andn2_b64 vcc, exec, s[46:47]
	s_waitcnt lgkmcnt(12)
	v_mfma_f32_32x32x16_bf16 v[84:99], v[152:155], v[100:103], v[68:83]
	v_mfma_f32_32x32x16_bf16 v[68:83], v[156:159], v[100:103], v[68:83]
	ds_read_b128 v[240:243], v2 offset:14336
	ds_read_b128 v[244:247], v2 offset:14848
	s_waitcnt lgkmcnt(12)
	v_mfma_f32_32x32x16_bf16 v[84:99], v[192:195], v[104:107], v[84:99]
	v_mfma_f32_32x32x16_bf16 v[68:83], v[196:199], v[104:107], v[68:83]
	s_waitcnt lgkmcnt(10)
	v_mfma_f32_32x32x16_bf16 v[84:99], v[200:203], v[108:111], v[84:99]
	v_mfma_f32_32x32x16_bf16 v[68:83], v[204:207], v[108:111], v[68:83]
	s_waitcnt lgkmcnt(8)
	v_mfma_f32_32x32x16_bf16 v[84:99], v[208:211], v[112:115], v[84:99]
	v_mfma_f32_32x32x16_bf16 v[68:83], v[212:215], v[112:115], v[68:83]
	s_waitcnt lgkmcnt(6)
	v_mfma_f32_32x32x16_bf16 v[84:99], v[216:219], v[116:119], v[84:99]
	v_mfma_f32_32x32x16_bf16 v[68:83], v[220:223], v[116:119], v[68:83]
	s_waitcnt lgkmcnt(4)
	v_mfma_f32_32x32x16_bf16 v[84:99], v[224:227], v[120:123], v[84:99]
	v_mfma_f32_32x32x16_bf16 v[68:83], v[228:231], v[120:123], v[68:83]
	s_waitcnt lgkmcnt(2)
	v_mfma_f32_32x32x16_bf16 v[84:99], v[232:235], v[124:127], v[84:99]
	v_mfma_f32_32x32x16_bf16 v[68:83], v[236:239], v[124:127], v[68:83]
	s_waitcnt lgkmcnt(0)
	v_mfma_f32_32x32x16_bf16 v[84:99], v[240:243], v[128:131], v[84:99]
	v_mfma_f32_32x32x16_bf16 v[68:83], v[244:247], v[128:131], v[68:83]
	s_nop 10
	v_max_f32_e32 v2, v85, v85
	v_max_f32_e32 v135, v84, v84
	v_max_f32_e32 v2, v135, v2
	v_max3_f32 v135, v86, v87, v69
	v_max3_f32 v2, v2, v68, v70
	v_max3_f32 v2, v2, v71, v88
	v_max3_f32 v135, v135, v90, v91
	v_max3_f32 v2, v2, v89, v72
	v_max3_f32 v135, v135, v74, v75
	v_max3_f32 v2, v2, v73, v92
	v_max3_f32 v135, v135, v94, v95
	v_max3_f32 v2, v2, v93, v76
	v_max3_f32 v135, v135, v78, v79
	v_max3_f32 v2, v2, v77, v96
	v_max3_f32 v135, v135, v98, v99
	v_max3_f32 v2, v2, v97, v80
	v_max3_f32 v135, v135, v82, v83
	v_max3_f32 v2, v2, v81, v135
	v_mov_b32_e32 v135, v2
	s_nop 1
	v_permlane32_swap_b32_e32 v2, v135
	v_max_f32_e32 v135, v135, v135
	v_max_f32_e32 v2, v2, v2
	v_max_f32_e32 v2, v2, v135
	v_cndmask_b32_e64 v135, 0, 1, s[46:47]
	v_cmp_ne_u32_e64 s[4:5], 1, v135
	s_mov_b64 s[46:47], s[44:45]
	s_cbranch_vccnz .LBB0_947
	v_cmp_lt_f32_e32 vcc, s50, v2
	s_cmp_lg_u64 vcc, 0
	s_cselect_b64 s[46:47], -1, 0
